# GEMM K-loops (in-proj, out-proj, PEER query): the per-segment s_setprio 1/0 toggles removed (48 instructions)
# speedup vs baseline: 1.0090x; 1.0008x over previous
; #define PG8_STAGE(bufoff, gbase, voff) do { _Pragma("unroll") for (int _i = 0; _i < 2; ++_i) { unsigned _vo = (voff)[_i]; asm volatile("" : "+v"(_vo));     \
;         __builtin_amdgcn_global_load_lds((const unsigned*)((const char*)(gbase) + _vo), (PG8_LAS unsigned*)(lds + (bufoff) + ldsw + _i * 8192), 16, 0, 0); } } while (0)
; #define PG8_LDA(dst, b, h) do { if constexpr (F8) { _Pragma("unroll") for (int m = 0; m < 4; ++m) dst##8[m] = PG8_LD8(lds + PG8_SA(b, h) + aoff + m * 2048); } \
;         else { _Pragma("unroll") for (int m = 0; m < 4; ++m) _Pragma("unroll") for (int k = 0; k < 2; ++k) dst[m][k] = *(const PG8_LAS bf16x8*)(lds + PG8_SA(b, h) + aoff + m * 2048 + k * 1024); } } while (0)
; #define PG8_LDB(dst, b, h) do { if constexpr (F8) { _Pragma("unroll") for (int n = 0; n < 2; ++n) dst##8[n] = PG8_LD8(lds + PG8_SB(b, h) + boff + n * 2048); } \
;         else { _Pragma("unroll") for (int n = 0; n < 2; ++n) _Pragma("unroll") for (int k = 0; k < 2; ++k) dst[n][k] = *(const PG8_LAS bf16x8*)(lds + PG8_SB(b, h) + boff + n * 2048 + k * 1024); } } while (0)
; #define PG8_WAIT_V(n) asm volatile("s_waitcnt vmcnt(" #n ")" ::: "memory")
; #define PG8_WAIT_L(n) asm volatile("s_waitcnt lgkmcnt(" #n ")" ::: "memory")
; #define PG8_BAR __builtin_amdgcn_s_barrier()
; #define PG8_SCHED __builtin_amdgcn_sched_barrier(0)
;     ...
;         for (int t = 0; t < nt; t += 2) {
;             const bool last = (t == nt - 2);
;             const char* a1 = cA + (size_t)(t + 1) * kstep;
;             const char* a2 = last ? nA : cA + (size_t)(t + 2) * kstep; const char* b2 = last ? nB : cB + (size_t)(t + 2) * kstep;
;             const char* a3 = a2 + kstep; const char* b3 = b2 + kstep;
;             if (last && has_next) S.a_ready(nxt);
;             if constexpr (SP2) {
;             PG8_LDB(B0, 0, 0); PG8_LDB(B1, 0, 1); PG8_SCHED; PG8_LDA(At, 0, 0); PG8_STAGE(PG8_SA(1, 1), a1 + hstep, voffA);
;             PG8_WAIT_V(8); PG8_WAIT_L(0); PG8_BAR; PG8_MMA(0, 0, At, B0); PG8_MMA(0, 1, At, B1); PG8_BAR; PG8_SCHED;
;             PG8_LDA(At, 0, 1); PG8_STAGE(PG8_SB(0, 0), b2, voffB); PG8_STAGE(PG8_SB(0, 1), b2 + hstep, voffB); PG8_STAGE(PG8_SA(0, 0), a2, voffA);
;             PG8_WAIT_V(8); PG8_WAIT_L(0); PG8_BAR; PG8_MMA(1, 0, At, B0); PG8_MMA(1, 1, At, B1); PG8_BAR; PG8_SCHED;
.LBB0_218:
	ds_read_b128 v[18:21], v167
	ds_read_b128 v[22:25], v167 offset:1024
	ds_read_b128 v[34:37], v167 offset:2048
	ds_read_b128 v[38:41], v167 offset:3072
	ds_read_b128 v[156:159], v168
	ds_read_b128 v[160:163], v168 offset:1024
	ds_read_b128 v[174:177], v168 offset:2048
	ds_read_b128 v[178:181], v168 offset:3072
	s_add_u32 s8, s4, 0xfffe0080
	s_addc_u32 s9, s5, -1
	s_cmp_eq_u32 s57, 4
	s_cselect_b32 s9, s0, s9
	s_cselect_b32 s8, s1, s8
	s_cselect_b32 s11, s33, s55
	s_cselect_b32 s10, s48, s49
	v_mov_b32_e32 v146, v1
	ds_read_b128 v[182:185], v169
	ds_read_b128 v[186:189], v169 offset:1024
	ds_read_b128 v[190:193], v169 offset:2048
	ds_read_b128 v[194:197], v169 offset:3072
	ds_read_b128 v[198:201], v169 offset:4096
	ds_read_b128 v[202:205], v169 offset:5120
	ds_read_b128 v[206:209], v169 offset:6144
	ds_read_b128 v[210:213], v169 offset:7168
	s_add_i32 m0, s15, 0xc000
	s_nop 0
	global_load_lds_dwordx4 v146, s[4:5]
	v_mov_b32_e32 v146, v164
	s_add_i32 m0, s15, 0xe000
	s_nop 0
	global_load_lds_dwordx4 v146, s[4:5]
	s_waitcnt vmcnt(8)
	s_waitcnt lgkmcnt(0)
	s_barrier
	s_waitcnt lgkmcnt(0)
	v_mfma_f32_16x16x128_f8f6f4 v[142:145], v[18:25], v[182:189], v[142:145]
	v_mfma_f32_16x16x128_f8f6f4 v[138:141], v[34:41], v[182:189], v[138:141]
	v_mfma_f32_16x16x128_f8f6f4 v[126:129], v[18:25], v[190:197], v[126:129]
	v_mfma_f32_16x16x128_f8f6f4 v[122:125], v[34:41], v[190:197], v[122:125]
	v_mfma_f32_16x16x128_f8f6f4 v[214:217], v[18:25], v[198:205], v[110:113]
	v_mfma_f32_16x16x128_f8f6f4 v[218:221], v[34:41], v[198:205], v[106:109]
	v_mfma_f32_16x16x128_f8f6f4 v[222:225], v[18:25], v[206:213], v[94:97]
	v_mfma_f32_16x16x128_f8f6f4 v[226:229], v[34:41], v[206:213], v[90:93]
	v_mfma_f32_16x16x128_f8f6f4 v[134:137], v[156:163], v[182:189], v[134:137]
	v_mfma_f32_16x16x128_f8f6f4 v[130:133], v[174:181], v[182:189], v[130:133]
	v_mfma_f32_16x16x128_f8f6f4 v[118:121], v[156:163], v[190:197], v[118:121]
	v_mfma_f32_16x16x128_f8f6f4 v[114:117], v[174:181], v[190:197], v[114:117]
	v_mfma_f32_16x16x128_f8f6f4 v[182:185], v[156:163], v[198:205], v[102:105]
	v_mfma_f32_16x16x128_f8f6f4 v[186:189], v[174:181], v[198:205], v[98:101]
	v_mfma_f32_16x16x128_f8f6f4 v[190:193], v[156:163], v[206:213], v[86:89]
	v_mfma_f32_16x16x128_f8f6f4 v[194:197], v[174:181], v[206:213], v[82:85]
	s_barrier
	v_mov_b32_e32 v146, v155
	s_add_i32 s62, s71, s39
	s_nop 2
	ds_read_b128 v[82:85], v169 offset:16384
	ds_read_b128 v[86:89], v169 offset:17408
	ds_read_b128 v[90:93], v169 offset:18432
	ds_read_b128 v[94:97], v169 offset:19456
	ds_read_b128 v[98:101], v169 offset:20480
	ds_read_b128 v[102:105], v169 offset:21504
	ds_read_b128 v[106:109], v169 offset:22528
	ds_read_b128 v[110:113], v169 offset:23552
	s_mov_b32 m0, s62
	s_nop 0
	global_load_lds_dwordx4 v146, s[10:11]
	v_mov_b32_e32 v146, v165
	s_add_i32 m0, s62, 0x2000
	s_add_u32 s62, s10, 0x20000
	global_load_lds_dwordx4 v146, s[10:11]
	s_addc_u32 s63, s11, 0
	v_mov_b32_e32 v146, v155
	s_add_i32 s64, s72, s39
	s_mov_b32 m0, s64
	s_nop 0
	global_load_lds_dwordx4 v146, s[62:63]
	v_mov_b32_e32 v146, v165
	s_add_i32 m0, s64, 0x2000
	s_nop 0
	global_load_lds_dwordx4 v146, s[62:63]
	v_mov_b32_e32 v146, v1
	s_mov_b32 m0, s15
	s_nop 0
	global_load_lds_dwordx4 v146, s[8:9]
	v_mov_b32_e32 v146, v164
	s_mov_b32 m0, s17
	s_nop 0
	global_load_lds_dwordx4 v146, s[8:9]
	s_waitcnt vmcnt(8)
	s_waitcnt lgkmcnt(0)
	s_barrier
	s_waitcnt lgkmcnt(0)
	v_mfma_f32_16x16x128_f8f6f4 v[78:81], v[18:25], v[82:89], v[78:81]
	v_mfma_f32_16x16x128_f8f6f4 v[74:77], v[34:41], v[82:89], v[74:77]
	v_mfma_f32_16x16x128_f8f6f4 v[62:65], v[18:25], v[90:97], v[62:65]
	v_mfma_f32_16x16x128_f8f6f4 v[58:61], v[34:41], v[90:97], v[58:61]
	v_mfma_f32_16x16x128_f8f6f4 v[198:201], v[18:25], v[98:105], v[46:49]
	v_mfma_f32_16x16x128_f8f6f4 v[202:205], v[34:41], v[98:105], v[42:45]
	v_mfma_f32_16x16x128_f8f6f4 v[206:209], v[18:25], v[106:113], v[14:17]
	v_mfma_f32_16x16x128_f8f6f4 v[210:213], v[34:41], v[106:113], v[10:13]
	v_mfma_f32_16x16x128_f8f6f4 v[70:73], v[156:163], v[82:89], v[70:73]
	v_mfma_f32_16x16x128_f8f6f4 v[66:69], v[174:181], v[82:89], v[66:69]
	v_mfma_f32_16x16x128_f8f6f4 v[230:233], v[156:163], v[90:97], v[54:57]
	v_mfma_f32_16x16x128_f8f6f4 v[234:237], v[174:181], v[90:97], v[50:53]
	v_mfma_f32_16x16x128_f8f6f4 v[238:241], v[156:163], v[98:105], v[30:33]
	v_mfma_f32_16x16x128_f8f6f4 v[242:245], v[174:181], v[98:105], v[26:29]
	v_mfma_f32_16x16x128_f8f6f4 v[246:249], v[156:163], v[106:113], v[6:9]
	v_mfma_f32_16x16x128_f8f6f4 v[250:253], v[174:181], v[106:113], v[2:5]
	s_barrier
; #define PG8_STAGE(bufoff, gbase, voff) do { _Pragma("unroll") for (int _i = 0; _i < 2; ++_i) { unsigned _vo = (voff)[_i]; asm volatile("" : "+v"(_vo));     \
;         __builtin_amdgcn_global_load_lds((const unsigned*)((const char*)(gbase) + _vo), (PG8_LAS unsigned*)(lds + (bufoff) + ldsw + _i * 8192), 16, 0, 0); } } while (0)
; #define PG8_LDA(dst, b, h) do { if constexpr (F8) { _Pragma("unroll") for (int m = 0; m < 4; ++m) dst##8[m] = PG8_LD8(lds + PG8_SA(b, h) + aoff + m * 2048); } \
;         else { _Pragma("unroll") for (int m = 0; m < 4; ++m) _Pragma("unroll") for (int k = 0; k < 2; ++k) dst[m][k] = *(const PG8_LAS bf16x8*)(lds + PG8_SA(b, h) + aoff + m * 2048 + k * 1024); } } while (0)
; #define PG8_LDB(dst, b, h) do { if constexpr (F8) { _Pragma("unroll") for (int n = 0; n < 2; ++n) dst##8[n] = PG8_LD8(lds + PG8_SB(b, h) + boff + n * 2048); } \
;         else { _Pragma("unroll") for (int n = 0; n < 2; ++n) _Pragma("unroll") for (int k = 0; k < 2; ++k) dst[n][k] = *(const PG8_LAS bf16x8*)(lds + PG8_SB(b, h) + boff + n * 2048 + k * 1024); } } while (0)
; #define PG8_WAIT_V(n) asm volatile("s_waitcnt vmcnt(" #n ")" ::: "memory")
; #define PG8_WAIT_L(n) asm volatile("s_waitcnt lgkmcnt(" #n ")" ::: "memory")
; #define PG8_BAR __builtin_amdgcn_s_barrier()
; #define PG8_SCHED __builtin_amdgcn_sched_barrier(0)
;     ...
;             PG8_LDB(B0, 1, 0); PG8_LDB(B1, 1, 1); PG8_SCHED; PG8_LDA(At, 1, 0); PG8_STAGE(PG8_SA(0, 1), a2 + hstep, voffA);
;             PG8_WAIT_V(8); PG8_WAIT_L(0); PG8_BAR; PG8_MMA(0, 0, At, B0); PG8_MMA(0, 1, At, B1); PG8_BAR; PG8_SCHED;
;             PG8_LDA(At, 1, 1); PG8_STAGE(PG8_SB(1, 0), b3, voffB); PG8_STAGE(PG8_SB(1, 1), b3 + hstep, voffB); PG8_STAGE(PG8_SA(1, 0), a3, voffA);
;             PG8_WAIT_V(8); PG8_WAIT_L(0); PG8_BAR; PG8_MMA(1, 0, At, B0); PG8_MMA(1, 1, At, B1); PG8_BAR; PG8_SCHED;
	s_add_i32 s64, 0, 0x18000
	v_add_u32_e32 v10, s64, v166
	s_add_i32 s65, 0, 0x1c000
	s_nop 1
	ds_read_b128 v[2:5], v10
	ds_read_b128 v[6:9], v10 offset:1024
	ds_read_b128 v[18:21], v10 offset:2048
	ds_read_b128 v[22:25], v10 offset:3072
	v_add_u32_e32 v10, s65, v166
	ds_read_b128 v[34:37], v10
	ds_read_b128 v[38:41], v10 offset:1024
	ds_read_b128 v[156:159], v10 offset:2048
	ds_read_b128 v[160:163], v10 offset:3072
	s_add_u32 s62, s8, 0x20000
	v_mov_b32_e32 v82, v1
	s_mov_b32 m0, s47
	ds_read_b128 v[10:13], v169 offset:32768
	ds_read_b128 v[14:17], v169 offset:33792
	ds_read_b128 v[26:29], v169 offset:34816
	ds_read_b128 v[30:33], v169 offset:35840
	ds_read_b128 v[42:45], v169 offset:36864
	ds_read_b128 v[46:49], v169 offset:37888
	ds_read_b128 v[50:53], v169 offset:38912
	ds_read_b128 v[54:57], v169 offset:39936
	s_addc_u32 s63, s9, 0
	s_nop 0
	global_load_lds_dwordx4 v82, s[62:63]
	v_mov_b32_e32 v82, v164
	s_mov_b32 m0, s50
	s_nop 0
	global_load_lds_dwordx4 v82, s[62:63]
	s_waitcnt vmcnt(8)
	s_waitcnt lgkmcnt(0)
	s_barrier
	s_waitcnt lgkmcnt(0)
	v_mfma_f32_16x16x128_f8f6f4 v[142:145], v[2:9], v[10:17], v[142:145]
	v_mfma_f32_16x16x128_f8f6f4 v[138:141], v[18:25], v[10:17], v[138:141]
	v_mfma_f32_16x16x128_f8f6f4 v[126:129], v[2:9], v[26:33], v[126:129]
	v_mfma_f32_16x16x128_f8f6f4 v[122:125], v[18:25], v[26:33], v[122:125]
	v_mfma_f32_16x16x128_f8f6f4 v[110:113], v[2:9], v[42:49], v[214:217]
	v_mfma_f32_16x16x128_f8f6f4 v[106:109], v[18:25], v[42:49], v[218:221]
	v_mfma_f32_16x16x128_f8f6f4 v[94:97], v[2:9], v[50:57], v[222:225]
	v_mfma_f32_16x16x128_f8f6f4 v[90:93], v[18:25], v[50:57], v[226:229]
	v_mfma_f32_16x16x128_f8f6f4 v[134:137], v[34:41], v[10:17], v[134:137]
	v_mfma_f32_16x16x128_f8f6f4 v[130:133], v[156:163], v[10:17], v[130:133]
	v_mfma_f32_16x16x128_f8f6f4 v[118:121], v[34:41], v[26:33], v[118:121]
	v_mfma_f32_16x16x128_f8f6f4 v[114:117], v[156:163], v[26:33], v[114:117]
	v_mfma_f32_16x16x128_f8f6f4 v[102:105], v[34:41], v[42:49], v[182:185]
	v_mfma_f32_16x16x128_f8f6f4 v[98:101], v[156:163], v[42:49], v[186:189]
	v_mfma_f32_16x16x128_f8f6f4 v[86:89], v[34:41], v[50:57], v[190:193]
	v_mfma_f32_16x16x128_f8f6f4 v[82:85], v[156:163], v[50:57], v[194:197]
	s_barrier
	v_mov_b32_e32 v146, v155
	ds_read_b128 v[26:29], v169 offset:49152
	ds_read_b128 v[30:33], v169 offset:50176
	ds_read_b128 v[174:177], v169 offset:51200
	ds_read_b128 v[178:181], v169 offset:52224
	ds_read_b128 v[182:185], v169 offset:53248
	ds_read_b128 v[186:189], v169 offset:54272
	ds_read_b128 v[190:193], v169 offset:55296
	ds_read_b128 v[194:197], v169 offset:56320
	s_add_i32 s62, s64, s39
	v_lshl_add_u64 v[10:11], s[10:11], 0, v[146:147]
	v_lshl_add_u64 v[10:11], v[10:11], 0, s[28:29]
	s_mov_b32 m0, s62
	v_mov_b32_e32 v146, v165
	global_load_lds_dwordx4 v[10:11], off
	s_add_i32 m0, s62, 0x2000
	v_lshl_add_u64 v[10:11], s[10:11], 0, v[146:147]
	v_lshl_add_u64 v[10:11], v[10:11], 0, s[28:29]
	s_add_u32 s10, s10, 0x20080
	global_load_lds_dwordx4 v[10:11], off
	s_addc_u32 s11, s11, 0
	v_mov_b32_e32 v10, v155
	s_add_i32 s62, s65, s39
	s_mov_b32 m0, s62
	v_mov_b32_e32 v146, v1
	global_load_lds_dwordx4 v10, s[10:11]
	v_mov_b32_e32 v10, v165
	s_add_i32 m0, s62, 0x2000
	s_nop 0
	global_load_lds_dwordx4 v10, s[10:11]
	s_mov_b32 m0, s68
	v_lshl_add_u64 v[10:11], s[8:9], 0, v[146:147]
	v_lshl_add_u64 v[10:11], v[10:11], 0, s[28:29]
	v_mov_b32_e32 v146, v164
	global_load_lds_dwordx4 v[10:11], off
	s_mov_b32 m0, s69
	v_lshl_add_u64 v[10:11], s[8:9], 0, v[146:147]
	v_lshl_add_u64 v[10:11], v[10:11], 0, s[28:29]
	global_load_lds_dwordx4 v[10:11], off
	s_waitcnt vmcnt(8)
	s_waitcnt lgkmcnt(0)
	s_barrier
	s_waitcnt lgkmcnt(0)
	v_mfma_f32_16x16x128_f8f6f4 v[78:81], v[2:9], v[26:33], v[78:81]
	v_mfma_f32_16x16x128_f8f6f4 v[74:77], v[18:25], v[26:33], v[74:77]
	v_mfma_f32_16x16x128_f8f6f4 v[62:65], v[2:9], v[174:181], v[62:65]
	v_mfma_f32_16x16x128_f8f6f4 v[58:61], v[18:25], v[174:181], v[58:61]
	v_mfma_f32_16x16x128_f8f6f4 v[46:49], v[2:9], v[182:189], v[198:201]
	v_mfma_f32_16x16x128_f8f6f4 v[42:45], v[18:25], v[182:189], v[202:205]
	v_mfma_f32_16x16x128_f8f6f4 v[14:17], v[2:9], v[190:197], v[206:209]
	v_mfma_f32_16x16x128_f8f6f4 v[10:13], v[18:25], v[190:197], v[210:213]
	v_mfma_f32_16x16x128_f8f6f4 v[70:73], v[34:41], v[26:33], v[70:73]
	v_mfma_f32_16x16x128_f8f6f4 v[66:69], v[156:163], v[26:33], v[66:69]
	v_mfma_f32_16x16x128_f8f6f4 v[54:57], v[34:41], v[174:181], v[230:233]
	v_mfma_f32_16x16x128_f8f6f4 v[50:53], v[156:163], v[174:181], v[234:237]
	v_mfma_f32_16x16x128_f8f6f4 v[30:33], v[34:41], v[182:189], v[238:241]
	v_mfma_f32_16x16x128_f8f6f4 v[26:29], v[156:163], v[182:189], v[242:245]
	v_mfma_f32_16x16x128_f8f6f4 v[6:9], v[34:41], v[190:197], v[246:249]
	v_mfma_f32_16x16x128_f8f6f4 v[2:5], v[156:163], v[190:197], v[250:253]
	s_barrier
	s_add_i32 s57, s57, 2
	s_add_u32 s4, s4, 0x100
	s_addc_u32 s5, s5, 0
	s_add_u32 s49, s49, 0x100
	s_addc_u32 s55, s55, 0
	s_cmp_gt_u32 s57, 5
	s_cbranch_scc0 .LBB0_218
	s_and_b64 vcc, exec, s[30:31]
	s_cbranch_vccz .LBB0_221
	s_barrier

; #define PG8_STAGE(bufoff, gbase, voff) do { _Pragma("unroll") for (int _i = 0; _i < 2; ++_i) { unsigned _vo = (voff)[_i]; asm volatile("" : "+v"(_vo));     \
;         __builtin_amdgcn_global_load_lds((const unsigned*)((const char*)(gbase) + _vo), (PG8_LAS unsigned*)(lds + (bufoff) + ldsw + _i * 8192), 16, 0, 0); } } while (0)
; #define PG8_LDA(dst, b, h) do { if constexpr (F8) { _Pragma("unroll") for (int m = 0; m < 4; ++m) dst##8[m] = PG8_LD8(lds + PG8_SA(b, h) + aoff + m * 2048); } \
;         else { _Pragma("unroll") for (int m = 0; m < 4; ++m) _Pragma("unroll") for (int k = 0; k < 2; ++k) dst[m][k] = *(const PG8_LAS bf16x8*)(lds + PG8_SA(b, h) + aoff + m * 2048 + k * 1024); } } while (0)
; #define PG8_LDB(dst, b, h) do { if constexpr (F8) { _Pragma("unroll") for (int n = 0; n < 2; ++n) dst##8[n] = PG8_LD8(lds + PG8_SB(b, h) + boff + n * 2048); } \
;         else { _Pragma("unroll") for (int n = 0; n < 2; ++n) _Pragma("unroll") for (int k = 0; k < 2; ++k) dst[n][k] = *(const PG8_LAS bf16x8*)(lds + PG8_SB(b, h) + boff + n * 2048 + k * 1024); } } while (0)
; #define PG8_WAIT_V(n) asm volatile("s_waitcnt vmcnt(" #n ")" ::: "memory")
; #define PG8_WAIT_L(n) asm volatile("s_waitcnt lgkmcnt(" #n ")" ::: "memory")
; #define PG8_BAR __builtin_amdgcn_s_barrier()
; #define PG8_SCHED __builtin_amdgcn_sched_barrier(0)
;     ...
;             PG8_LDB(B0, 0, 0); PG8_LDB(B1, 0, 1); PG8_SCHED; PG8_LDA(At, 0, 0); PG8_STAGE(PG8_SA(1, 1), a1 + hstep, voffA);
;             PG8_WAIT_V(8); PG8_WAIT_L(0); PG8_BAR; PG8_MMA(0, 0, At, B0); PG8_MMA(0, 1, At, B1); PG8_BAR; PG8_SCHED;
;             PG8_LDA(At, 0, 1); PG8_STAGE(PG8_SB(0, 0), b2, voffB); PG8_STAGE(PG8_SB(0, 1), b2 + hstep, voffB); PG8_STAGE(PG8_SA(0, 0), a2, voffA);
;             PG8_WAIT_V(8); PG8_WAIT_L(0); PG8_BAR; PG8_MMA(1, 0, At, B0); PG8_MMA(1, 1, At, B1); PG8_BAR; PG8_SCHED;
.LBB0_701:
	ds_read_b128 v[144:147], v140
	ds_read_b128 v[148:151], v140 offset:1024
	ds_read_b128 v[152:155], v140 offset:2048
	ds_read_b128 v[156:159], v140 offset:3072
	ds_read_b128 v[160:163], v141
	ds_read_b128 v[164:167], v141 offset:1024
	ds_read_b128 v[168:171], v141 offset:2048
	ds_read_b128 v[172:175], v141 offset:3072
	s_add_u32 s40, s38, 0xfffe0080
	s_addc_u32 s41, s39, -1
	s_cmp_eq_u32 s64, 4
	s_cselect_b32 s41, s0, s41
	s_cselect_b32 s40, s1, s40
	s_cselect_b32 s45, s27, s63
	s_cselect_b32 s44, s29, s62
	v_mov_b32_e32 v130, v1
	ds_read_b128 v[176:179], v142
	ds_read_b128 v[180:183], v142 offset:1024
	ds_read_b128 v[184:187], v142 offset:2048
	ds_read_b128 v[188:191], v142 offset:3072
	ds_read_b128 v[192:195], v142 offset:4096
	ds_read_b128 v[196:199], v142 offset:5120
	ds_read_b128 v[200:203], v142 offset:6144
	ds_read_b128 v[204:207], v142 offset:7168
	s_add_i32 m0, s37, 0xc000
	s_nop 0
	global_load_lds_dwordx4 v130, s[38:39]
	v_mov_b32_e32 v130, v137
	s_add_i32 m0, s37, 0xe000
	s_nop 0
	global_load_lds_dwordx4 v130, s[38:39]
	s_waitcnt vmcnt(8)
	s_waitcnt lgkmcnt(0)
	s_barrier
	s_waitcnt lgkmcnt(0)
	v_mfma_f32_16x16x128_f8f6f4 v[126:129], v[144:151], v[176:183], v[126:129]
	v_mfma_f32_16x16x128_f8f6f4 v[122:125], v[152:159], v[176:183], v[122:125]
	v_mfma_f32_16x16x128_f8f6f4 v[114:117], v[144:151], v[184:191], v[114:117]
	v_mfma_f32_16x16x128_f8f6f4 v[106:109], v[152:159], v[184:191], v[106:109]
	v_mfma_f32_16x16x128_f8f6f4 v[98:101], v[144:151], v[192:199], v[98:101]
	v_mfma_f32_16x16x128_f8f6f4 v[208:211], v[152:159], v[192:199], v[90:93]
	v_mfma_f32_16x16x128_f8f6f4 v[212:215], v[144:151], v[200:207], v[82:85]
	v_mfma_f32_16x16x128_f8f6f4 v[216:219], v[152:159], v[200:207], v[74:77]
	v_mfma_f32_16x16x128_f8f6f4 v[118:121], v[160:167], v[176:183], v[118:121]
	v_mfma_f32_16x16x128_f8f6f4 v[110:113], v[168:175], v[176:183], v[110:113]
	v_mfma_f32_16x16x128_f8f6f4 v[102:105], v[160:167], v[184:191], v[102:105]
	v_mfma_f32_16x16x128_f8f6f4 v[176:179], v[168:175], v[184:191], v[94:97]
	v_mfma_f32_16x16x128_f8f6f4 v[180:183], v[160:167], v[192:199], v[86:89]
	v_mfma_f32_16x16x128_f8f6f4 v[184:187], v[168:175], v[192:199], v[78:81]
	v_mfma_f32_16x16x128_f8f6f4 v[188:191], v[160:167], v[200:207], v[70:73]
	v_mfma_f32_16x16x128_f8f6f4 v[192:195], v[168:175], v[200:207], v[66:69]
	s_barrier
	v_mov_b32_e32 v130, v136
	s_add_i32 s65, s55, s48
	s_nop 2
	ds_read_b128 v[66:69], v142 offset:16384
	ds_read_b128 v[70:73], v142 offset:17408
	ds_read_b128 v[74:77], v142 offset:18432
	ds_read_b128 v[78:81], v142 offset:19456
	ds_read_b128 v[82:85], v142 offset:20480
	ds_read_b128 v[86:89], v142 offset:21504
	ds_read_b128 v[90:93], v142 offset:22528
	ds_read_b128 v[94:97], v142 offset:23552
	s_mov_b32 m0, s65
	s_nop 0
	global_load_lds_dwordx4 v130, s[44:45]
	v_mov_b32_e32 v130, v138
	s_add_i32 m0, s65, 0x2000
	s_add_u32 s66, s44, 0x20000
	global_load_lds_dwordx4 v130, s[44:45]
	s_addc_u32 s67, s45, 0
	v_mov_b32_e32 v130, v136
	s_add_i32 s65, s56, s48
	s_mov_b32 m0, s65
	s_nop 0
	global_load_lds_dwordx4 v130, s[66:67]
	v_mov_b32_e32 v130, v138
	s_add_i32 m0, s65, 0x2000
	s_nop 0
	global_load_lds_dwordx4 v130, s[66:67]
	v_mov_b32_e32 v130, v1
	s_mov_b32 m0, s37
	s_nop 0
	global_load_lds_dwordx4 v130, s[40:41]
	v_mov_b32_e32 v130, v137
	s_mov_b32 m0, s49
	s_nop 0
	global_load_lds_dwordx4 v130, s[40:41]
	s_waitcnt vmcnt(8)
	s_waitcnt lgkmcnt(0)
	s_barrier
	s_waitcnt lgkmcnt(0)
	v_mfma_f32_16x16x128_f8f6f4 v[62:65], v[144:151], v[66:73], v[62:65]
	v_mfma_f32_16x16x128_f8f6f4 v[58:61], v[152:159], v[66:73], v[58:61]
	v_mfma_f32_16x16x128_f8f6f4 v[50:53], v[144:151], v[74:81], v[50:53]
	v_mfma_f32_16x16x128_f8f6f4 v[196:199], v[152:159], v[74:81], v[42:45]
	v_mfma_f32_16x16x128_f8f6f4 v[200:203], v[144:151], v[82:89], v[34:37]
	v_mfma_f32_16x16x128_f8f6f4 v[204:207], v[152:159], v[82:89], v[26:29]
	v_mfma_f32_16x16x128_f8f6f4 v[220:223], v[144:151], v[90:97], v[18:21]
	v_mfma_f32_16x16x128_f8f6f4 v[224:227], v[152:159], v[90:97], v[10:13]
	v_mfma_f32_16x16x128_f8f6f4 v[54:57], v[160:167], v[66:73], v[54:57]
	v_mfma_f32_16x16x128_f8f6f4 v[228:231], v[168:175], v[66:73], v[46:49]
	v_mfma_f32_16x16x128_f8f6f4 v[232:235], v[160:167], v[74:81], v[38:41]
	v_mfma_f32_16x16x128_f8f6f4 v[236:239], v[168:175], v[74:81], v[30:33]
	v_mfma_f32_16x16x128_f8f6f4 v[240:243], v[160:167], v[82:89], v[22:25]
	v_mfma_f32_16x16x128_f8f6f4 v[244:247], v[168:175], v[82:89], v[14:17]
	v_mfma_f32_16x16x128_f8f6f4 v[248:251], v[160:167], v[90:97], v[6:9]
	v_mfma_f32_16x16x128_f8f6f4 v[132:135], v[168:175], v[90:97], v[2:5]
	s_barrier
; #define PG8_STAGE(bufoff, gbase, voff) do { _Pragma("unroll") for (int _i = 0; _i < 2; ++_i) { unsigned _vo = (voff)[_i]; asm volatile("" : "+v"(_vo));     \
;         __builtin_amdgcn_global_load_lds((const unsigned*)((const char*)(gbase) + _vo), (PG8_LAS unsigned*)(lds + (bufoff) + ldsw + _i * 8192), 16, 0, 0); } } while (0)
; #define PG8_LDA(dst, b, h) do { if constexpr (F8) { _Pragma("unroll") for (int m = 0; m < 4; ++m) dst##8[m] = PG8_LD8(lds + PG8_SA(b, h) + aoff + m * 2048); } \
;         else { _Pragma("unroll") for (int m = 0; m < 4; ++m) _Pragma("unroll") for (int k = 0; k < 2; ++k) dst[m][k] = *(const PG8_LAS bf16x8*)(lds + PG8_SA(b, h) + aoff + m * 2048 + k * 1024); } } while (0)
; #define PG8_LDB(dst, b, h) do { if constexpr (F8) { _Pragma("unroll") for (int n = 0; n < 2; ++n) dst##8[n] = PG8_LD8(lds + PG8_SB(b, h) + boff + n * 2048); } \
;         else { _Pragma("unroll") for (int n = 0; n < 2; ++n) _Pragma("unroll") for (int k = 0; k < 2; ++k) dst[n][k] = *(const PG8_LAS bf16x8*)(lds + PG8_SB(b, h) + boff + n * 2048 + k * 1024); } } while (0)
; #define PG8_WAIT_V(n) asm volatile("s_waitcnt vmcnt(" #n ")" ::: "memory")
; #define PG8_WAIT_L(n) asm volatile("s_waitcnt lgkmcnt(" #n ")" ::: "memory")
; #define PG8_BAR __builtin_amdgcn_s_barrier()
; #define PG8_SCHED __builtin_amdgcn_sched_barrier(0)
;     ...
;         for (int t = 0; t < nt; t += 2) {
;     ...
;             PG8_LDB(B0, 1, 0); PG8_LDB(B1, 1, 1); PG8_SCHED; PG8_LDA(At, 1, 0); PG8_STAGE(PG8_SA(0, 1), a2 + hstep, voffA);
;             PG8_WAIT_V(8); PG8_WAIT_L(0); PG8_BAR; PG8_MMA(0, 0, At, B0); PG8_MMA(0, 1, At, B1); PG8_BAR; PG8_SCHED;
;             PG8_LDA(At, 1, 1); PG8_STAGE(PG8_SB(1, 0), b3, voffB); PG8_STAGE(PG8_SB(1, 1), b3 + hstep, voffB); PG8_STAGE(PG8_SA(1, 0), a3, voffA);
;             PG8_WAIT_V(8); PG8_WAIT_L(0); PG8_BAR; PG8_MMA(1, 0, At, B0); PG8_MMA(1, 1, At, B1); PG8_BAR; PG8_SCHED;
	s_add_i32 s65, 0, 0x18000
	s_add_i32 s68, 0, 0x1c000
	s_nop 0
	v_add_u32_e32 v14, s65, v139
	v_add_u32_e32 v18, s68, v139
	ds_read_b128 v[2:5], v14
	ds_read_b128 v[6:9], v14 offset:1024
	ds_read_b128 v[10:13], v14 offset:2048
	ds_read_b128 v[14:17], v14 offset:3072
	ds_read_b128 v[144:147], v18
	ds_read_b128 v[148:151], v18 offset:1024
	ds_read_b128 v[152:155], v18 offset:2048
	ds_read_b128 v[156:159], v18 offset:3072
	s_add_u32 s66, s40, 0x20000
	v_mov_b32_e32 v66, v1
	s_mov_b32 m0, s50
	ds_read_b128 v[18:21], v142 offset:32768
	ds_read_b128 v[22:25], v142 offset:33792
	ds_read_b128 v[26:29], v142 offset:34816
	ds_read_b128 v[30:33], v142 offset:35840
	ds_read_b128 v[34:37], v142 offset:36864
	ds_read_b128 v[38:41], v142 offset:37888
	ds_read_b128 v[42:45], v142 offset:38912
	ds_read_b128 v[46:49], v142 offset:39936
	s_addc_u32 s67, s41, 0
	s_nop 0
	global_load_lds_dwordx4 v66, s[66:67]
	v_mov_b32_e32 v66, v137
	s_mov_b32 m0, s51
	s_nop 0
	global_load_lds_dwordx4 v66, s[66:67]
	s_waitcnt vmcnt(8)
	s_waitcnt lgkmcnt(0)
	s_barrier
	s_waitcnt lgkmcnt(0)
	v_mfma_f32_16x16x128_f8f6f4 v[126:129], v[2:9], v[18:25], v[126:129]
	v_mfma_f32_16x16x128_f8f6f4 v[122:125], v[10:17], v[18:25], v[122:125]
	v_mfma_f32_16x16x128_f8f6f4 v[114:117], v[2:9], v[26:33], v[114:117]
	v_mfma_f32_16x16x128_f8f6f4 v[106:109], v[10:17], v[26:33], v[106:109]
	v_mfma_f32_16x16x128_f8f6f4 v[98:101], v[2:9], v[34:41], v[98:101]
	v_mfma_f32_16x16x128_f8f6f4 v[90:93], v[10:17], v[34:41], v[208:211]
	v_mfma_f32_16x16x128_f8f6f4 v[82:85], v[2:9], v[42:49], v[212:215]
	v_mfma_f32_16x16x128_f8f6f4 v[74:77], v[10:17], v[42:49], v[216:219]
	v_mfma_f32_16x16x128_f8f6f4 v[118:121], v[144:151], v[18:25], v[118:121]
	v_mfma_f32_16x16x128_f8f6f4 v[110:113], v[152:159], v[18:25], v[110:113]
	v_mfma_f32_16x16x128_f8f6f4 v[102:105], v[144:151], v[26:33], v[102:105]
	v_mfma_f32_16x16x128_f8f6f4 v[94:97], v[152:159], v[26:33], v[176:179]
	v_mfma_f32_16x16x128_f8f6f4 v[86:89], v[144:151], v[34:41], v[180:183]
	v_mfma_f32_16x16x128_f8f6f4 v[78:81], v[152:159], v[34:41], v[184:187]
	v_mfma_f32_16x16x128_f8f6f4 v[70:73], v[144:151], v[42:49], v[188:191]
	v_mfma_f32_16x16x128_f8f6f4 v[66:69], v[152:159], v[42:49], v[192:195]
	s_barrier
	v_mov_b32_e32 v130, v136
	ds_read_b128 v[160:163], v142 offset:49152
	ds_read_b128 v[164:167], v142 offset:50176
	ds_read_b128 v[168:171], v142 offset:51200
	ds_read_b128 v[172:175], v142 offset:52224
	ds_read_b128 v[176:179], v142 offset:53248
	ds_read_b128 v[180:183], v142 offset:54272
	ds_read_b128 v[184:187], v142 offset:55296
	ds_read_b128 v[188:191], v142 offset:56320
	s_add_i32 s65, s65, s48
	v_lshl_add_u64 v[18:19], s[44:45], 0, v[130:131]
	v_lshl_add_u64 v[18:19], v[18:19], 0, s[14:15]
	s_mov_b32 m0, s65
	v_mov_b32_e32 v130, v138
	global_load_lds_dwordx4 v[18:19], off
	s_add_i32 m0, s65, 0x2000
	v_lshl_add_u64 v[18:19], s[44:45], 0, v[130:131]
	v_lshl_add_u64 v[18:19], v[18:19], 0, s[14:15]
	s_add_u32 s44, s44, 0x20080
	global_load_lds_dwordx4 v[18:19], off
	s_addc_u32 s45, s45, 0
	v_mov_b32_e32 v18, v136
	s_add_i32 s65, s68, s48
	s_mov_b32 m0, s65
	v_mov_b32_e32 v130, v1
	global_load_lds_dwordx4 v18, s[44:45]
	v_mov_b32_e32 v18, v138
	s_add_i32 m0, s65, 0x2000
	s_nop 0
	global_load_lds_dwordx4 v18, s[44:45]
	s_mov_b32 m0, s53
	v_lshl_add_u64 v[18:19], s[40:41], 0, v[130:131]
	v_lshl_add_u64 v[18:19], v[18:19], 0, s[14:15]
	v_mov_b32_e32 v130, v137
	global_load_lds_dwordx4 v[18:19], off
	s_mov_b32 m0, s54
	v_lshl_add_u64 v[18:19], s[40:41], 0, v[130:131]
	v_lshl_add_u64 v[18:19], v[18:19], 0, s[14:15]
	global_load_lds_dwordx4 v[18:19], off
	s_waitcnt vmcnt(8)
	s_waitcnt lgkmcnt(0)
	s_barrier
	s_waitcnt lgkmcnt(0)
	v_mfma_f32_16x16x128_f8f6f4 v[62:65], v[2:9], v[160:167], v[62:65]
	v_mfma_f32_16x16x128_f8f6f4 v[58:61], v[10:17], v[160:167], v[58:61]
	v_mfma_f32_16x16x128_f8f6f4 v[50:53], v[2:9], v[168:175], v[50:53]
	v_mfma_f32_16x16x128_f8f6f4 v[42:45], v[10:17], v[168:175], v[196:199]
	v_mfma_f32_16x16x128_f8f6f4 v[34:37], v[2:9], v[176:183], v[200:203]
	v_mfma_f32_16x16x128_f8f6f4 v[26:29], v[10:17], v[176:183], v[204:207]
	v_mfma_f32_16x16x128_f8f6f4 v[18:21], v[2:9], v[184:191], v[220:223]
	v_mfma_f32_16x16x128_f8f6f4 v[10:13], v[10:17], v[184:191], v[224:227]
	v_mfma_f32_16x16x128_f8f6f4 v[54:57], v[144:151], v[160:167], v[54:57]
	v_mfma_f32_16x16x128_f8f6f4 v[46:49], v[152:159], v[160:167], v[228:231]
	v_mfma_f32_16x16x128_f8f6f4 v[38:41], v[144:151], v[168:175], v[232:235]
	v_mfma_f32_16x16x128_f8f6f4 v[30:33], v[152:159], v[168:175], v[236:239]
	v_mfma_f32_16x16x128_f8f6f4 v[22:25], v[144:151], v[176:183], v[240:243]
	v_mfma_f32_16x16x128_f8f6f4 v[14:17], v[152:159], v[176:183], v[244:247]
	v_mfma_f32_16x16x128_f8f6f4 v[6:9], v[144:151], v[184:191], v[248:251]
	v_mfma_f32_16x16x128_f8f6f4 v[2:5], v[152:159], v[184:191], v[132:135]
	s_barrier
	s_add_i32 s64, s64, 2
	s_add_u32 s38, s38, 0x100
	s_addc_u32 s39, s39, 0
	s_add_u32 s62, s62, 0x100
	s_addc_u32 s63, s63, 0
	s_cmp_gt_u32 s64, 5
	s_cbranch_scc0 .LBB0_701
	s_and_b64 vcc, exec, s[16:17]
	s_cbranch_vccz .LBB0_704
	s_barrier

; #define PG8_STAGE(bufoff, gbase, voff) do { _Pragma("unroll") for (int _i = 0; _i < 2; ++_i) { unsigned _vo = (voff)[_i]; asm volatile("" : "+v"(_vo));     \
;         __builtin_amdgcn_global_load_lds((const unsigned*)((const char*)(gbase) + _vo), (PG8_LAS unsigned*)(lds + (bufoff) + ldsw + _i * 8192), 16, 0, 0); } } while (0)
; #define PG8_LDA(dst, b, h) do { if constexpr (F8) { _Pragma("unroll") for (int m = 0; m < 4; ++m) dst##8[m] = PG8_LD8(lds + PG8_SA(b, h) + aoff + m * 2048); } \
;         else { _Pragma("unroll") for (int m = 0; m < 4; ++m) _Pragma("unroll") for (int k = 0; k < 2; ++k) dst[m][k] = *(const PG8_LAS bf16x8*)(lds + PG8_SA(b, h) + aoff + m * 2048 + k * 1024); } } while (0)
; #define PG8_LDB(dst, b, h) do { if constexpr (F8) { _Pragma("unroll") for (int n = 0; n < 2; ++n) dst##8[n] = PG8_LD8(lds + PG8_SB(b, h) + boff + n * 2048); } \
;         else { _Pragma("unroll") for (int n = 0; n < 2; ++n) _Pragma("unroll") for (int k = 0; k < 2; ++k) dst[n][k] = *(const PG8_LAS bf16x8*)(lds + PG8_SB(b, h) + boff + n * 2048 + k * 1024); } } while (0)
; #define PG8_WAIT_V(n) asm volatile("s_waitcnt vmcnt(" #n ")" ::: "memory")
; #define PG8_WAIT_L(n) asm volatile("s_waitcnt lgkmcnt(" #n ")" ::: "memory")
; #define PG8_BAR __builtin_amdgcn_s_barrier()
; #define PG8_SCHED __builtin_amdgcn_sched_barrier(0)
;     ...
;             PG8_LDB(B0, 0, 0); PG8_LDB(B1, 0, 1); PG8_SCHED; PG8_LDA(At, 0, 0); PG8_STAGE(PG8_SA(1, 1), a1 + hstep, voffA);
;             PG8_WAIT_V(8); PG8_WAIT_L(0); PG8_BAR; PG8_MMA(0, 0, At, B0); PG8_MMA(0, 1, At, B1); PG8_BAR; PG8_SCHED;
;             PG8_LDA(At, 0, 1); PG8_STAGE(PG8_SB(0, 0), b2, voffB); PG8_STAGE(PG8_SB(0, 1), b2 + hstep, voffB); PG8_STAGE(PG8_SA(0, 0), a2, voffA);
;             PG8_WAIT_V(8); PG8_WAIT_L(0); PG8_BAR; PG8_MMA(1, 0, At, B0); PG8_MMA(1, 1, At, B1); PG8_BAR; PG8_SCHED;
.LBB0_838:
	ds_read_b128 v[136:139], v148
	ds_read_b128 v[140:143], v148 offset:1024
	ds_read_b128 v[152:155], v148 offset:2048
	ds_read_b128 v[156:159], v148 offset:3072
	ds_read_b128 v[160:163], v149
	ds_read_b128 v[164:167], v149 offset:1024
	ds_read_b128 v[168:171], v149 offset:2048
	ds_read_b128 v[172:175], v149 offset:3072
	s_add_u32 s44, s40, 0xfffe0080
	s_addc_u32 s45, s41, -1
	s_cmp_eq_u32 s66, 4
	s_cselect_b32 s45, s0, s45
	s_cselect_b32 s44, s1, s44
	s_cselect_b32 s47, s5, s65
	s_cselect_b32 s46, s31, s49
	v_mov_b32_e32 v130, v1
	ds_read_b128 v[176:179], v150
	ds_read_b128 v[180:183], v150 offset:1024
	ds_read_b128 v[184:187], v150 offset:2048
	ds_read_b128 v[188:191], v150 offset:3072
	ds_read_b128 v[192:195], v150 offset:4096
	ds_read_b128 v[196:199], v150 offset:5120
	ds_read_b128 v[200:203], v150 offset:6144
	ds_read_b128 v[204:207], v150 offset:7168
	s_add_i32 m0, s39, 0xc000
	s_nop 0
	global_load_lds_dwordx4 v130, s[40:41]
	v_mov_b32_e32 v130, v145
	s_add_i32 m0, s39, 0xe000
	s_nop 0
	global_load_lds_dwordx4 v130, s[40:41]
	s_waitcnt vmcnt(8)
	s_waitcnt lgkmcnt(0)
	s_barrier
	s_waitcnt lgkmcnt(0)
	v_mfma_i32_16x16x64_i8 v[126:129], v[136:139], v[176:179], v[126:129]
	v_mfma_i32_16x16x64_i8 v[122:125], v[152:155], v[176:179], v[122:125]
	v_mfma_i32_16x16x64_i8 v[110:113], v[136:139], v[184:187], v[110:113]
	v_mfma_i32_16x16x64_i8 v[106:109], v[152:155], v[184:187], v[106:109]
	v_mfma_i32_16x16x64_i8 v[94:97], v[136:139], v[192:195], v[94:97]
	v_mfma_i32_16x16x64_i8 v[90:93], v[152:155], v[192:195], v[90:93]
	v_mfma_i32_16x16x64_i8 v[78:81], v[136:139], v[200:203], v[78:81]
	v_mfma_i32_16x16x64_i8 v[74:77], v[152:155], v[200:203], v[74:77]
	v_mfma_i32_16x16x64_i8 v[126:129], v[140:143], v[180:183], v[126:129]
	v_mfma_i32_16x16x64_i8 v[122:125], v[156:159], v[180:183], v[122:125]
	v_mfma_i32_16x16x64_i8 v[110:113], v[140:143], v[188:191], v[110:113]
	v_mfma_i32_16x16x64_i8 v[106:109], v[156:159], v[188:191], v[106:109]
	v_mfma_i32_16x16x64_i8 v[94:97], v[140:143], v[196:199], v[94:97]
	v_mfma_i32_16x16x64_i8 v[90:93], v[156:159], v[196:199], v[90:93]
	v_mfma_i32_16x16x64_i8 v[78:81], v[140:143], v[204:207], v[78:81]
	v_mfma_i32_16x16x64_i8 v[74:77], v[156:159], v[204:207], v[74:77]
	v_mfma_i32_16x16x64_i8 v[118:121], v[160:163], v[176:179], v[118:121]
	v_mfma_i32_16x16x64_i8 v[114:117], v[168:171], v[176:179], v[114:117]
	v_mfma_i32_16x16x64_i8 v[102:105], v[160:163], v[184:187], v[102:105]
	v_mfma_i32_16x16x64_i8 v[98:101], v[168:171], v[184:187], v[98:101]
	v_mfma_i32_16x16x64_i8 v[86:89], v[160:163], v[192:195], v[86:89]
	v_mfma_i32_16x16x64_i8 v[82:85], v[168:171], v[192:195], v[82:85]
	v_mfma_i32_16x16x64_i8 v[70:73], v[160:163], v[200:203], v[70:73]
	v_mfma_i32_16x16x64_i8 v[66:69], v[168:171], v[200:203], v[66:69]
	v_mfma_i32_16x16x64_i8 v[118:121], v[164:167], v[180:183], v[118:121]
	v_mfma_i32_16x16x64_i8 v[114:117], v[172:175], v[180:183], v[114:117]
	v_mfma_i32_16x16x64_i8 v[102:105], v[164:167], v[188:191], v[102:105]
	v_mfma_i32_16x16x64_i8 v[98:101], v[172:175], v[188:191], v[98:101]
	v_mfma_i32_16x16x64_i8 v[86:89], v[164:167], v[196:199], v[86:89]
	v_mfma_i32_16x16x64_i8 v[82:85], v[172:175], v[196:199], v[82:85]
	v_mfma_i32_16x16x64_i8 v[70:73], v[164:167], v[204:207], v[70:73]
	v_mfma_i32_16x16x64_i8 v[66:69], v[172:175], v[204:207], v[66:69]
	s_barrier
	v_mov_b32_e32 v130, v144
	s_add_i32 s67, s59, s53
	ds_read_b128 v[176:179], v150 offset:16384
	ds_read_b128 v[180:183], v150 offset:17408
	ds_read_b128 v[184:187], v150 offset:18432
	ds_read_b128 v[188:191], v150 offset:19456
	ds_read_b128 v[192:195], v150 offset:20480
	ds_read_b128 v[196:199], v150 offset:21504
	ds_read_b128 v[200:203], v150 offset:22528
	ds_read_b128 v[204:207], v150 offset:23552
	s_mov_b32 m0, s67
	s_nop 0
	global_load_lds_dwordx4 v130, s[46:47]
	v_mov_b32_e32 v130, v146
	s_add_i32 m0, s67, 0x2000
	s_add_u32 s68, s46, 0x20000
	global_load_lds_dwordx4 v130, s[46:47]
	s_addc_u32 s69, s47, 0
	v_mov_b32_e32 v130, v144
	s_add_i32 s67, s60, s53
	s_mov_b32 m0, s67
	s_nop 0
	global_load_lds_dwordx4 v130, s[68:69]
	v_mov_b32_e32 v130, v146
	s_add_i32 m0, s67, 0x2000
	s_nop 0
	global_load_lds_dwordx4 v130, s[68:69]
	v_mov_b32_e32 v130, v1
	s_mov_b32 m0, s39
	s_nop 0
	global_load_lds_dwordx4 v130, s[44:45]
	v_mov_b32_e32 v130, v145
	s_mov_b32 m0, s33
	s_nop 0
	global_load_lds_dwordx4 v130, s[44:45]
	s_waitcnt vmcnt(8)
	s_waitcnt lgkmcnt(0)
	s_barrier
	s_waitcnt lgkmcnt(0)
	v_mfma_i32_16x16x64_i8 v[62:65], v[136:139], v[176:179], v[62:65]
	v_mfma_i32_16x16x64_i8 v[58:61], v[152:155], v[176:179], v[58:61]
	v_mfma_i32_16x16x64_i8 v[46:49], v[136:139], v[184:187], v[46:49]
	v_mfma_i32_16x16x64_i8 v[42:45], v[152:155], v[184:187], v[42:45]
	v_mfma_i32_16x16x64_i8 v[30:33], v[136:139], v[192:195], v[30:33]
	v_mfma_i32_16x16x64_i8 v[26:29], v[152:155], v[192:195], v[26:29]
	v_mfma_i32_16x16x64_i8 v[14:17], v[136:139], v[200:203], v[14:17]
	v_mfma_i32_16x16x64_i8 v[10:13], v[152:155], v[200:203], v[10:13]
	v_mfma_i32_16x16x64_i8 v[62:65], v[140:143], v[180:183], v[62:65]
	v_mfma_i32_16x16x64_i8 v[58:61], v[156:159], v[180:183], v[58:61]
	v_mfma_i32_16x16x64_i8 v[46:49], v[140:143], v[188:191], v[46:49]
	v_mfma_i32_16x16x64_i8 v[42:45], v[156:159], v[188:191], v[42:45]
	v_mfma_i32_16x16x64_i8 v[30:33], v[140:143], v[196:199], v[30:33]
	v_mfma_i32_16x16x64_i8 v[26:29], v[156:159], v[196:199], v[26:29]
	v_mfma_i32_16x16x64_i8 v[14:17], v[140:143], v[204:207], v[14:17]
	v_mfma_i32_16x16x64_i8 v[10:13], v[156:159], v[204:207], v[10:13]
	v_mfma_i32_16x16x64_i8 v[54:57], v[160:163], v[176:179], v[54:57]
	v_mfma_i32_16x16x64_i8 v[50:53], v[168:171], v[176:179], v[50:53]
	v_mfma_i32_16x16x64_i8 v[38:41], v[160:163], v[184:187], v[38:41]
	v_mfma_i32_16x16x64_i8 v[34:37], v[168:171], v[184:187], v[34:37]
	v_mfma_i32_16x16x64_i8 v[22:25], v[160:163], v[192:195], v[22:25]
	v_mfma_i32_16x16x64_i8 v[18:21], v[168:171], v[192:195], v[18:21]
	v_mfma_i32_16x16x64_i8 v[6:9], v[160:163], v[200:203], v[6:9]
	v_mfma_i32_16x16x64_i8 v[2:5], v[168:171], v[200:203], v[2:5]
	v_mfma_i32_16x16x64_i8 v[54:57], v[164:167], v[180:183], v[54:57]
	v_mfma_i32_16x16x64_i8 v[50:53], v[172:175], v[180:183], v[50:53]
	v_mfma_i32_16x16x64_i8 v[38:41], v[164:167], v[188:191], v[38:41]
	v_mfma_i32_16x16x64_i8 v[34:37], v[172:175], v[188:191], v[34:37]
	v_mfma_i32_16x16x64_i8 v[22:25], v[164:167], v[196:199], v[22:25]
	v_mfma_i32_16x16x64_i8 v[18:21], v[172:175], v[196:199], v[18:21]
	v_mfma_i32_16x16x64_i8 v[6:9], v[164:167], v[204:207], v[6:9]
	v_mfma_i32_16x16x64_i8 v[2:5], v[172:175], v[204:207], v[2:5]
	s_barrier
; #define PG8_STAGE(bufoff, gbase, voff) do { _Pragma("unroll") for (int _i = 0; _i < 2; ++_i) { unsigned _vo = (voff)[_i]; asm volatile("" : "+v"(_vo));     \
;         __builtin_amdgcn_global_load_lds((const unsigned*)((const char*)(gbase) + _vo), (PG8_LAS unsigned*)(lds + (bufoff) + ldsw + _i * 8192), 16, 0, 0); } } while (0)
; #define PG8_LDA(dst, b, h) do { if constexpr (F8) { _Pragma("unroll") for (int m = 0; m < 4; ++m) dst##8[m] = PG8_LD8(lds + PG8_SA(b, h) + aoff + m * 2048); } \
;         else { _Pragma("unroll") for (int m = 0; m < 4; ++m) _Pragma("unroll") for (int k = 0; k < 2; ++k) dst[m][k] = *(const PG8_LAS bf16x8*)(lds + PG8_SA(b, h) + aoff + m * 2048 + k * 1024); } } while (0)
; #define PG8_LDB(dst, b, h) do { if constexpr (F8) { _Pragma("unroll") for (int n = 0; n < 2; ++n) dst##8[n] = PG8_LD8(lds + PG8_SB(b, h) + boff + n * 2048); } \
;         else { _Pragma("unroll") for (int n = 0; n < 2; ++n) _Pragma("unroll") for (int k = 0; k < 2; ++k) dst[n][k] = *(const PG8_LAS bf16x8*)(lds + PG8_SB(b, h) + boff + n * 2048 + k * 1024); } } while (0)
; #define PG8_WAIT_V(n) asm volatile("s_waitcnt vmcnt(" #n ")" ::: "memory")
; #define PG8_WAIT_L(n) asm volatile("s_waitcnt lgkmcnt(" #n ")" ::: "memory")
; #define PG8_BAR __builtin_amdgcn_s_barrier()
; #define PG8_SCHED __builtin_amdgcn_sched_barrier(0)
;     ...
;             PG8_LDB(B0, 1, 0); PG8_LDB(B1, 1, 1); PG8_SCHED; PG8_LDA(At, 1, 0); PG8_STAGE(PG8_SA(0, 1), a2 + hstep, voffA);
;             PG8_WAIT_V(8); PG8_WAIT_L(0); PG8_BAR; PG8_MMA(0, 0, At, B0); PG8_MMA(0, 1, At, B1); PG8_BAR; PG8_SCHED;
	s_add_i32 s67, 0, 0x18000
	v_add_u32_e32 v130, s67, v147
	s_add_i32 s70, 0, 0x1c000
	ds_read_b128 v[136:139], v130
	ds_read_b128 v[140:143], v130 offset:1024
	ds_read_b128 v[152:155], v130 offset:2048
	ds_read_b128 v[156:159], v130 offset:3072
	v_add_u32_e32 v130, s70, v147
	ds_read_b128 v[160:163], v130
	ds_read_b128 v[164:167], v130 offset:1024
	ds_read_b128 v[168:171], v130 offset:2048
	ds_read_b128 v[172:175], v130 offset:3072
	s_add_u32 s68, s44, 0x20000
	v_mov_b32_e32 v130, v1
	s_mov_b32 m0, s54
	ds_read_b128 v[176:179], v150 offset:32768
	ds_read_b128 v[180:183], v150 offset:33792
	ds_read_b128 v[184:187], v150 offset:34816
	ds_read_b128 v[188:191], v150 offset:35840
	ds_read_b128 v[192:195], v150 offset:36864
	ds_read_b128 v[196:199], v150 offset:37888
	ds_read_b128 v[200:203], v150 offset:38912
	ds_read_b128 v[204:207], v150 offset:39936
	s_addc_u32 s69, s45, 0
	s_nop 0
	global_load_lds_dwordx4 v130, s[68:69]
	v_mov_b32_e32 v130, v145
	s_mov_b32 m0, s55
	s_nop 0
	global_load_lds_dwordx4 v130, s[68:69]
	s_waitcnt vmcnt(8)
	s_waitcnt lgkmcnt(0)
	s_barrier
	s_waitcnt lgkmcnt(0)
	v_mfma_i32_16x16x64_i8 v[126:129], v[136:139], v[176:179], v[126:129]
	v_mfma_i32_16x16x64_i8 v[122:125], v[152:155], v[176:179], v[122:125]
	v_mfma_i32_16x16x64_i8 v[110:113], v[136:139], v[184:187], v[110:113]
	v_mfma_i32_16x16x64_i8 v[106:109], v[152:155], v[184:187], v[106:109]
	v_mfma_i32_16x16x64_i8 v[94:97], v[136:139], v[192:195], v[94:97]
	v_mfma_i32_16x16x64_i8 v[90:93], v[152:155], v[192:195], v[90:93]
	v_mfma_i32_16x16x64_i8 v[78:81], v[136:139], v[200:203], v[78:81]
	v_mfma_i32_16x16x64_i8 v[74:77], v[152:155], v[200:203], v[74:77]
	v_mfma_i32_16x16x64_i8 v[126:129], v[140:143], v[180:183], v[126:129]
	v_mfma_i32_16x16x64_i8 v[122:125], v[156:159], v[180:183], v[122:125]
	v_mfma_i32_16x16x64_i8 v[110:113], v[140:143], v[188:191], v[110:113]
	v_mfma_i32_16x16x64_i8 v[106:109], v[156:159], v[188:191], v[106:109]
	v_mfma_i32_16x16x64_i8 v[94:97], v[140:143], v[196:199], v[94:97]
	v_mfma_i32_16x16x64_i8 v[90:93], v[156:159], v[196:199], v[90:93]
	v_mfma_i32_16x16x64_i8 v[78:81], v[140:143], v[204:207], v[78:81]
	v_mfma_i32_16x16x64_i8 v[74:77], v[156:159], v[204:207], v[74:77]
	v_mfma_i32_16x16x64_i8 v[118:121], v[160:163], v[176:179], v[118:121]
	v_mfma_i32_16x16x64_i8 v[114:117], v[168:171], v[176:179], v[114:117]
	v_mfma_i32_16x16x64_i8 v[102:105], v[160:163], v[184:187], v[102:105]
	v_mfma_i32_16x16x64_i8 v[98:101], v[168:171], v[184:187], v[98:101]
	v_mfma_i32_16x16x64_i8 v[86:89], v[160:163], v[192:195], v[86:89]
	v_mfma_i32_16x16x64_i8 v[82:85], v[168:171], v[192:195], v[82:85]
	v_mfma_i32_16x16x64_i8 v[70:73], v[160:163], v[200:203], v[70:73]
	v_mfma_i32_16x16x64_i8 v[66:69], v[168:171], v[200:203], v[66:69]
	v_mfma_i32_16x16x64_i8 v[118:121], v[164:167], v[180:183], v[118:121]
	v_mfma_i32_16x16x64_i8 v[114:117], v[172:175], v[180:183], v[114:117]
	v_mfma_i32_16x16x64_i8 v[102:105], v[164:167], v[188:191], v[102:105]
	v_mfma_i32_16x16x64_i8 v[98:101], v[172:175], v[188:191], v[98:101]
	v_mfma_i32_16x16x64_i8 v[86:89], v[164:167], v[196:199], v[86:89]
	v_mfma_i32_16x16x64_i8 v[82:85], v[172:175], v[196:199], v[82:85]
	v_mfma_i32_16x16x64_i8 v[70:73], v[164:167], v[204:207], v[70:73]
	v_mfma_i32_16x16x64_i8 v[66:69], v[172:175], v[204:207], v[66:69]
	s_barrier
; #define PG8_STAGE(bufoff, gbase, voff) do { _Pragma("unroll") for (int _i = 0; _i < 2; ++_i) { unsigned _vo = (voff)[_i]; asm volatile("" : "+v"(_vo));     \
;         __builtin_amdgcn_global_load_lds((const unsigned*)((const char*)(gbase) + _vo), (PG8_LAS unsigned*)(lds + (bufoff) + ldsw + _i * 8192), 16, 0, 0); } } while (0)
; #define PG8_LDA(dst, b, h) do { if constexpr (F8) { _Pragma("unroll") for (int m = 0; m < 4; ++m) dst##8[m] = PG8_LD8(lds + PG8_SA(b, h) + aoff + m * 2048); } \
;         else { _Pragma("unroll") for (int m = 0; m < 4; ++m) _Pragma("unroll") for (int k = 0; k < 2; ++k) dst[m][k] = *(const PG8_LAS bf16x8*)(lds + PG8_SA(b, h) + aoff + m * 2048 + k * 1024); } } while (0)
; #define PG8_WAIT_V(n) asm volatile("s_waitcnt vmcnt(" #n ")" ::: "memory")
; #define PG8_WAIT_L(n) asm volatile("s_waitcnt lgkmcnt(" #n ")" ::: "memory")
; #define PG8_BAR __builtin_amdgcn_s_barrier()
; #define PG8_SCHED __builtin_amdgcn_sched_barrier(0)
;     ...
;         for (int t = 0; t < nt; t += 2) {
;     ...
;             PG8_LDA(At, 1, 1); PG8_STAGE(PG8_SB(1, 0), b3, voffB); PG8_STAGE(PG8_SB(1, 1), b3 + hstep, voffB); PG8_STAGE(PG8_SA(1, 0), a3, voffA);
;             PG8_WAIT_V(8); PG8_WAIT_L(0); PG8_BAR; PG8_MMA(1, 0, At, B0); PG8_MMA(1, 1, At, B1); PG8_BAR; PG8_SCHED;
	v_mov_b32_e32 v130, v144
	ds_read_b128 v[176:179], v150 offset:49152
	ds_read_b128 v[180:183], v150 offset:50176
	ds_read_b128 v[184:187], v150 offset:51200
	ds_read_b128 v[188:191], v150 offset:52224
	ds_read_b128 v[192:195], v150 offset:53248
	ds_read_b128 v[196:199], v150 offset:54272
	ds_read_b128 v[200:203], v150 offset:55296
	ds_read_b128 v[204:207], v150 offset:56320
	s_add_i32 s67, s67, s53
	v_lshl_add_u64 v[208:209], s[46:47], 0, v[130:131]
	v_lshl_add_u64 v[208:209], v[208:209], 0, s[16:17]
	s_mov_b32 m0, s67
	v_mov_b32_e32 v130, v146
	global_load_lds_dwordx4 v[208:209], off
	s_add_i32 m0, s67, 0x2000
	s_nop 0
	v_lshl_add_u64 v[208:209], s[46:47], 0, v[130:131]
	s_add_u32 s46, s46, 0x20080
	v_lshl_add_u64 v[208:209], v[208:209], 0, s[16:17]
	s_addc_u32 s47, s47, 0
	v_mov_b32_e32 v130, v144
	s_add_i32 s67, s70, s53
	global_load_lds_dwordx4 v[208:209], off
	s_mov_b32 m0, s67
	s_nop 0
	global_load_lds_dwordx4 v130, s[46:47]
	v_mov_b32_e32 v130, v146
	s_add_i32 m0, s67, 0x2000
	s_nop 0
	global_load_lds_dwordx4 v130, s[46:47]
	v_mov_b32_e32 v130, v1
	s_mov_b32 m0, s57
	v_lshl_add_u64 v[208:209], s[44:45], 0, v[130:131]
	v_lshl_add_u64 v[208:209], v[208:209], 0, s[16:17]
	v_mov_b32_e32 v130, v145
	global_load_lds_dwordx4 v[208:209], off
	s_mov_b32 m0, s58
	v_lshl_add_u64 v[208:209], s[44:45], 0, v[130:131]
	v_lshl_add_u64 v[208:209], v[208:209], 0, s[16:17]
	global_load_lds_dwordx4 v[208:209], off
	s_waitcnt vmcnt(8)
	s_waitcnt lgkmcnt(0)
	s_barrier
	s_waitcnt lgkmcnt(0)
	v_mfma_i32_16x16x64_i8 v[62:65], v[136:139], v[176:179], v[62:65]
	v_mfma_i32_16x16x64_i8 v[58:61], v[152:155], v[176:179], v[58:61]
	v_mfma_i32_16x16x64_i8 v[46:49], v[136:139], v[184:187], v[46:49]
	v_mfma_i32_16x16x64_i8 v[42:45], v[152:155], v[184:187], v[42:45]
	v_mfma_i32_16x16x64_i8 v[30:33], v[136:139], v[192:195], v[30:33]
	v_mfma_i32_16x16x64_i8 v[26:29], v[152:155], v[192:195], v[26:29]
	v_mfma_i32_16x16x64_i8 v[14:17], v[136:139], v[200:203], v[14:17]
	v_mfma_i32_16x16x64_i8 v[10:13], v[152:155], v[200:203], v[10:13]
	v_mfma_i32_16x16x64_i8 v[62:65], v[140:143], v[180:183], v[62:65]
	v_mfma_i32_16x16x64_i8 v[58:61], v[156:159], v[180:183], v[58:61]
	v_mfma_i32_16x16x64_i8 v[46:49], v[140:143], v[188:191], v[46:49]
	v_mfma_i32_16x16x64_i8 v[42:45], v[156:159], v[188:191], v[42:45]
	v_mfma_i32_16x16x64_i8 v[30:33], v[140:143], v[196:199], v[30:33]
	v_mfma_i32_16x16x64_i8 v[26:29], v[156:159], v[196:199], v[26:29]
	v_mfma_i32_16x16x64_i8 v[14:17], v[140:143], v[204:207], v[14:17]
	v_mfma_i32_16x16x64_i8 v[10:13], v[156:159], v[204:207], v[10:13]
	v_mfma_i32_16x16x64_i8 v[54:57], v[160:163], v[176:179], v[54:57]
	v_mfma_i32_16x16x64_i8 v[50:53], v[168:171], v[176:179], v[50:53]
	v_mfma_i32_16x16x64_i8 v[38:41], v[160:163], v[184:187], v[38:41]
	v_mfma_i32_16x16x64_i8 v[34:37], v[168:171], v[184:187], v[34:37]
	v_mfma_i32_16x16x64_i8 v[22:25], v[160:163], v[192:195], v[22:25]
	v_mfma_i32_16x16x64_i8 v[18:21], v[168:171], v[192:195], v[18:21]
	v_mfma_i32_16x16x64_i8 v[6:9], v[160:163], v[200:203], v[6:9]
	v_mfma_i32_16x16x64_i8 v[2:5], v[168:171], v[200:203], v[2:5]
	v_mfma_i32_16x16x64_i8 v[54:57], v[164:167], v[180:183], v[54:57]
	v_mfma_i32_16x16x64_i8 v[50:53], v[172:175], v[180:183], v[50:53]
	v_mfma_i32_16x16x64_i8 v[38:41], v[164:167], v[188:191], v[38:41]
	v_mfma_i32_16x16x64_i8 v[34:37], v[172:175], v[188:191], v[34:37]
	v_mfma_i32_16x16x64_i8 v[22:25], v[164:167], v[196:199], v[22:25]
	v_mfma_i32_16x16x64_i8 v[18:21], v[172:175], v[196:199], v[18:21]
	v_mfma_i32_16x16x64_i8 v[6:9], v[164:167], v[204:207], v[6:9]
	v_mfma_i32_16x16x64_i8 v[2:5], v[172:175], v[204:207], v[2:5]
	s_barrier
	s_add_i32 s66, s66, 2
	s_add_u32 s40, s40, 0x100
	s_addc_u32 s41, s41, 0
	s_add_u32 s49, s49, 0x100
	s_addc_u32 s65, s65, 0
	s_cmp_gt_u32 s66, 5
	s_cbranch_scc0 .LBB0_838
	s_and_b64 vcc, exec, s[18:19]
	s_cbranch_vccz .LBB0_841
	s_barrier
